# U phase: packed-word stores of a 4-token group staged in spare LDS and written as two coalesced 16-byte-per-slot stores (waves 0-6)
# speedup vs baseline: 1.0097x; 1.0097x over previous
; #define LAS __attribute__((address_space(3)))
; template <int VAR> __device__ __forceinline__ void u_process_grp(const UGrp& d, const v4u (&xb)[16], int j, size_t t0, int lane, LAS unsigned char* wl, const unsigned char* __restrict__ UT, const float* __restrict__ egate, unsigned* __restrict__ PW) {
;     ...
;         dv *= __uint_as_float((ent >> 24) << 23) * 0.125f;
;         const pg8::f32x2 gl = pg8::gelu_pk((pg8::f32x2){dv, dv});
;         const float wv = gl.x * gate;
;         if (VAR != 3 && pl < n) PW[(blk * 128 + slot) * 64 + tk0 + tkk] = (__float_as_uint(wv) & 0xFFFE0000u) | ((ent & 0x3FFFu) << 3);
; template <int VAR> __device__ __forceinline__ void peer_u_phase(int wave, int grp, int gwl  , LAS unsigned char* lds, gu32* qhead  , const unsigned char* __restrict__ X1Q, const unsigned char* __restrict__ UT, ...
;     ...
;         for (int h = 0; h < 2; ++h) {
;             v4u xb[16];
; #pragma unroll
;             for (int k = 0; k < 4; ++k) *((LAS v4u*)(wl + k * 1024) + lane) = h == 0 ? da.xq[k] : db.xq[k];
;             asm volatile("s_waitcnt lgkmcnt(0)" ::: "memory");
; #pragma unroll
;             for (int i = 0; i < 16; ++i) xb[i] = *(const LAS v4u*)(wl + (lane & 3) * 1024 + 256 * (lane >> 4) + 16 * i);
;             asm volatile("s_waitcnt lgkmcnt(0)" ::: "memory");
; #pragma unroll 1
;             for (int r = 0; r < 8; ++r) {
;                 const int j = ((h == 0 ? r : 7 - r) + grp) & 7;
;                 if (h == 0) u_process_grp<VAR>(da, xb, j, t0, lane, wl, UT, egate, PW); else u_process_grp<VAR>(db, xb, j, t0 + 4, lane, wl, UT, egate, PW);
;             }
;         }
.LBB0_669:
	s_cmp_eq_u32 s61, 7
	s_cbranch_scc1 .Lpwf_0
	s_mov_b64 s[34:35], exec
	s_mov_b64 exec, -1
	s_cmp_lg_u64 s[44:45], 0
	s_cselect_b32 s98, s20, s18
	s_cselect_b32 s99, s21, s19
	v_mbcnt_lo_u32_b32 v124, -1, 0
	v_mbcnt_hi_u32_b32 v124, -1, v124
	v_mov_b32_e32 v126, s61
	v_lshlrev_b32_e32 v125, 4, v124
	v_lshl_add_u32 v125, v126, 11, v125
	v_add_u32_e32 v125, 0x24000, v125
	s_waitcnt lgkmcnt(0)
	ds_read_b128 v[56:59], v125
	ds_read_b128 v[60:63], v125 offset:1024
	v_or_b32_e32 v120, s27, v124
	v_mov_b32_e32 v121, s15
	v_lshlrev_b64 v[120:121], 8, v[120:121]
	v_lshl_add_u64 v[120:121], s[98:99], 0, v[120:121]
	s_mov_b64 s[98:99], 0x4000
	v_lshl_add_u64 v[122:123], v[120:121], 0, s[98:99]
	s_waitcnt lgkmcnt(0)
	global_store_dwordx4 v[120:121], v[56:59], off
	global_store_dwordx4 v[122:123], v[60:63], off
	s_mov_b64 exec, s[34:35]

; template <int VAR> __device__ __forceinline__ void u_process_grp(const UGrp& d, const v4u (&xb)[16], int j, size_t t0, int lane, LAS unsigned char* wl, const unsigned char* __restrict__ UT, const float* __restrict__ egate, unsigned* __restrict__ PW) {
;     ...
;         dv *= __uint_as_float((ent >> 24) << 23) * 0.125f;
;         const pg8::f32x2 gl = pg8::gelu_pk((pg8::f32x2){dv, dv});
;         const float wv = gl.x * gate;
;         if (VAR != 3 && pl < n) PW[(blk * 128 + slot) * 64 + tk0 + tkk] = (__float_as_uint(wv) & 0xFFFE0000u) | ((ent & 0x3FFFu) << 3);
.LBB0_749:
	s_and_saveexec_b64 s[6:7], vcc
	s_cbranch_execz .LBB0_707
	v_lshlrev_b32_sdwa v96, v229, v231 dst_sel:DWORD dst_unused:UNUSED_PAD src0_sel:DWORD src1_sel:BYTE_3
	v_mul_f32_e32 v96, 0x3e000000, v96
	v_mul_f32_e32 v96, v96, v233
	s_waitcnt lgkmcnt(1)
	v_and_b32_e32 v98, 0x7fffffff, v96
	s_waitcnt lgkmcnt(0)
	v_pk_fma_f32 v[98:99], v[98:99], s[22:23], 1.0 op_sel_hi:[0,0,0]
	v_rcp_f32_e32 v98, v98
	v_rcp_f32_e32 v99, v99
	v_mul_f32_e32 v100, v96, v96
	v_mul_f32_e32 v100, 0xbf38aa3b, v100
	v_exp_f32_e32 v100, v100
	v_pk_fma_f32 v[102:103], v[98:99], s[24:25], v[176:177] op_sel_hi:[1,0,0]
	v_bfe_u32 v97, v231, 14, 7
	v_pk_fma_f32 v[102:103], v[98:99], v[102:103], s[26:27] op_sel_hi:[1,1,0]
	v_cmp_gt_f32_e32 vcc, 0, v96
	v_pk_fma_f32 v[102:103], v[98:99], v[102:103], s[28:29] op_sel_hi:[1,1,0]
	v_lshlrev_b32_e32 v140, 2, v178
	v_pk_fma_f32 v[102:103], v[98:99], v[102:103], s[42:43] op_sel_hi:[1,1,0]
	s_nop 0
	v_pk_mul_f32 v[98:99], v[98:99], v[102:103]
	s_nop 0
	v_pk_mul_f32 v[98:99], v[100:101], v[98:99] op_sel_hi:[0,1]
	v_mul_f32_e32 v100, v96, v98
	v_pk_fma_f32 v[98:99], v[96:97], v[98:99], v[96:97] op_sel_hi:[0,1,1] neg_lo:[1,0,0] neg_hi:[1,0,0]
	v_cndmask_b32_e32 v96, v98, v100, vcc
	v_lshlrev_b32_e32 v98, 3, v231
	s_waitcnt vmcnt(0)
	v_mul_f32_e32 v96, v232, v96
	v_and_b32_e32 v98, 0x1fff8, v98
	v_and_or_b32 v98, v96, s43, v98
	s_cmp_eq_u32 s61, 7
	s_cbranch_scc1 .Lpwd_0
	s_lshl_b32 s98, s61, 11
	s_add_i32 s98, s98, 0x24000
	v_and_b32_e32 v96, 12, v140
	v_lshl_add_u32 v96, v97, 4, v96
	v_add_u32_e32 v96, s98, v96
	ds_write_b32 v96, v98
	s_branch .LBB0_707
.Lpwd_0:
	v_or_b32_e32 v96, s27, v97
	v_mov_b32_e32 v97, s15
	v_lshlrev_b64 v[96:97], 8, v[96:97]
	v_lshl_add_u64 v[96:97], s[18:19], 0, v[96:97]
	v_lshl_add_u64 v[96:97], v[96:97], 0, v[140:141]
	global_store_dword v[96:97], v98, off
	s_branch .LBB0_707

; template <int VAR> __device__ __forceinline__ void u_process_grp(const UGrp& d, const v4u (&xb)[16], int j, size_t t0, int lane, LAS unsigned char* wl, const unsigned char* __restrict__ UT, const float* __restrict__ egate, unsigned* __restrict__ PW) {
;     ...
;         dv *= __uint_as_float((ent >> 24) << 23) * 0.125f;
;         const pg8::f32x2 gl = pg8::gelu_pk((pg8::f32x2){dv, dv});
;         const float wv = gl.x * gate;
;         if (VAR != 3 && pl < n) PW[(blk * 128 + slot) * 64 + tk0 + tkk] = (__float_as_uint(wv) & 0xFFFE0000u) | ((ent & 0x3FFFu) << 3);
.LBB0_829:
	s_and_saveexec_b64 s[6:7], vcc
	s_cbranch_execz .LBB0_787
	v_lshlrev_b32_sdwa v96, v229, v231 dst_sel:DWORD dst_unused:UNUSED_PAD src0_sel:DWORD src1_sel:BYTE_3
	v_mul_f32_e32 v96, 0x3e000000, v96
	v_mul_f32_e32 v96, v96, v232
	s_waitcnt lgkmcnt(1)
	v_and_b32_e32 v98, 0x7fffffff, v96
	s_waitcnt lgkmcnt(0)
	v_pk_fma_f32 v[98:99], v[98:99], s[22:23], 1.0 op_sel_hi:[0,0,0]
	v_rcp_f32_e32 v98, v98
	v_rcp_f32_e32 v99, v99
	v_mul_f32_e32 v100, v96, v96
	v_mul_f32_e32 v100, 0xbf38aa3b, v100
	v_exp_f32_e32 v100, v100
	v_pk_fma_f32 v[102:103], v[98:99], s[24:25], v[176:177] op_sel_hi:[1,0,0]
	v_bfe_u32 v97, v231, 14, 7
	v_pk_fma_f32 v[102:103], v[98:99], v[102:103], s[26:27] op_sel_hi:[1,1,0]
	v_cmp_gt_f32_e32 vcc, 0, v96
	v_pk_fma_f32 v[102:103], v[98:99], v[102:103], s[28:29] op_sel_hi:[1,1,0]
	v_lshlrev_b32_e32 v140, 2, v178
	v_pk_fma_f32 v[102:103], v[98:99], v[102:103], s[42:43] op_sel_hi:[1,1,0]
	s_nop 0
	v_pk_mul_f32 v[98:99], v[98:99], v[102:103]
	s_nop 0
	v_pk_mul_f32 v[98:99], v[100:101], v[98:99] op_sel_hi:[0,1]
	v_mul_f32_e32 v100, v96, v98
	v_pk_fma_f32 v[98:99], v[96:97], v[98:99], v[96:97] op_sel_hi:[0,1,1] neg_lo:[1,0,0] neg_hi:[1,0,0]
	v_cndmask_b32_e32 v96, v98, v100, vcc
	v_lshlrev_b32_e32 v98, 3, v231
	s_waitcnt vmcnt(0)
	v_mul_f32_e32 v96, v179, v96
	v_and_b32_e32 v98, 0x1fff8, v98
	v_and_or_b32 v98, v96, s43, v98
	s_cmp_eq_u32 s61, 7
	s_cbranch_scc1 .Lpwd_1
	s_lshl_b32 s98, s61, 11
	s_add_i32 s98, s98, 0x24000
	v_and_b32_e32 v96, 12, v140
	v_lshl_add_u32 v96, v97, 4, v96
	v_add_u32_e32 v96, s98, v96
	ds_write_b32 v96, v98
	s_branch .LBB0_787
.Lpwd_1:
	v_or_b32_e32 v96, s27, v97
	v_mov_b32_e32 v97, s15
	v_lshlrev_b64 v[96:97], 8, v[96:97]
	v_lshl_add_u64 v[96:97], s[20:21], 0, v[96:97]
	v_lshl_add_u64 v[96:97], v[96:97], 0, v[140:141]
	global_store_dword v[96:97], v98, off
	s_branch .LBB0_787
